# baseline (speedup 1.0000x reference)
_Z15score_ds_kernelPKfS0_S0_S0_S0_S0_PfPKDF16_:
	s_load_dwordx4 s[8:11], s[0:1], 0x0
	s_and_b32 s16, s2, 7
	s_bfe_u32 s14, s2, 0x10003
	s_cmp_eq_u32 s14, 0
	s_cselect_b64 s[12:13], -1, 0
	s_and_b64 s[4:5], s[12:13], exec
	s_mul_i32 s3, s16, 0x9600
	v_and_b32_e32 v206, 15, v0
	v_bfe_u32 v207, v0, 6, 2
	s_waitcnt lgkmcnt(0)
	s_cselect_b32 s4, s9, s11
	s_cselect_b32 s5, s8, s10
	s_lshl_b32 s3, s3, 2
	v_bfe_u32 v208, v0, 4, 2
	v_lshl_or_b32 v1, v207, 5, v206
	s_add_u32 s6, s5, s3
	v_lshlrev_b32_e32 v209, 3, v208
	v_mul_u32_u24_e32 v76, 0x12c, v1
	s_addc_u32 s7, s4, 0
	v_add_lshl_u32 v202, v209, v76, 2
	global_load_dwordx4 v[66:69], v202, s[6:7] offset:16
	global_load_dwordx4 v[70:73], v202, s[6:7]
	global_load_dwordx4 v[58:61], v202, s[6:7] offset:144
	global_load_dwordx4 v[62:65], v202, s[6:7] offset:128
	global_load_dwordx4 v[50:53], v202, s[6:7] offset:272
	global_load_dwordx4 v[54:57], v202, s[6:7] offset:256
	global_load_dwordx4 v[42:45], v202, s[6:7] offset:400
	global_load_dwordx4 v[46:49], v202, s[6:7] offset:384
	global_load_dwordx4 v[34:37], v202, s[6:7] offset:528
	global_load_dwordx4 v[38:41], v202, s[6:7] offset:512
	global_load_dwordx4 v[26:29], v202, s[6:7] offset:656
	global_load_dwordx4 v[30:33], v202, s[6:7] offset:640
	global_load_dwordx4 v[18:21], v202, s[6:7] offset:784
	global_load_dwordx4 v[22:25], v202, s[6:7] offset:768
	global_load_dwordx4 v[10:13], v202, s[6:7] offset:912
	global_load_dwordx4 v[14:17], v202, s[6:7] offset:896
	global_load_dwordx4 v[2:5], v202, s[6:7] offset:1040
	global_load_dwordx4 v[6:9], v202, s[6:7] offset:1024
	s_movk_i32 s8, 0x12c
	v_mov_b32_e32 v203, 0
	v_or_b32_e32 v1, 0x120, v209
	v_lshl_add_u64 v[74:75], s[6:7], 0, v[202:203]
	v_cmp_gt_u32_e32 vcc, s8, v1
	v_mov_b32_e32 v210, 0
	v_mov_b32_e32 v211, 0
	v_mov_b32_e32 v212, 0
	v_mov_b32_e32 v230, 0
	v_mov_b32_e32 v231, 0
	v_mov_b32_e32 v232, 0
	v_mov_b32_e32 v233, 0
	v_mov_b32_e32 v234, 0
	v_mov_b32_e32 v235, 0
	v_mov_b32_e32 v236, 0
	v_mov_b32_e32 v237, 0
	v_mov_b32_e32 v238, 0
	v_mov_b32_e32 v239, 0
	v_mov_b32_e32 v240, 0
	v_mov_b32_e32 v241, 0
	v_mov_b32_e32 v242, 0
	v_mov_b32_e32 v243, 0
	v_mov_b32_e32 v244, 0
	v_mov_b32_e32 v245, 0
	s_and_saveexec_b64 s[4:5], vcc
	s_cbranch_execz .LBB1_2
	global_load_dwordx4 v[230:233], v[74:75], off offset:1152
.LBB1_2:
	s_or_b64 exec, exec, s[4:5]
	v_or_b32_e32 v1, 0x124, v209
	v_cmp_gt_u32_e64 s[4:5], s8, v1
	v_mov_b32_e32 v1, 0
	s_and_saveexec_b64 s[8:9], s[4:5]
	s_cbranch_execz .LBB1_4
	global_load_dwordx4 v[234:237], v[74:75], off offset:1168
.LBB1_4:
	s_or_b64 exec, exec, s[8:9]
	v_add_u32_e32 v74, v76, v209
	v_mov_b32_e32 v75, 0x4b00
	v_lshl_add_u32 v204, v74, 2, v75
	global_load_dwordx4 v[138:141], v204, s[6:7] offset:16
	global_load_dwordx4 v[142:145], v204, s[6:7]
	global_load_dwordx4 v[130:133], v204, s[6:7] offset:144
	global_load_dwordx4 v[134:137], v204, s[6:7] offset:128
	global_load_dwordx4 v[122:125], v204, s[6:7] offset:272
	global_load_dwordx4 v[126:129], v204, s[6:7] offset:256
	global_load_dwordx4 v[114:117], v204, s[6:7] offset:400
	global_load_dwordx4 v[118:121], v204, s[6:7] offset:384
	global_load_dwordx4 v[106:109], v204, s[6:7] offset:528
	global_load_dwordx4 v[110:113], v204, s[6:7] offset:512
	global_load_dwordx4 v[98:101], v204, s[6:7] offset:656
	global_load_dwordx4 v[102:105], v204, s[6:7] offset:640
	global_load_dwordx4 v[90:93], v204, s[6:7] offset:784
	global_load_dwordx4 v[94:97], v204, s[6:7] offset:768
	global_load_dwordx4 v[82:85], v204, s[6:7] offset:912
	global_load_dwordx4 v[86:89], v204, s[6:7] offset:896
	global_load_dwordx4 v[74:77], v204, s[6:7] offset:1040
	global_load_dwordx4 v[78:81], v204, s[6:7] offset:1024
	s_load_dwordx2 s[8:9], s[0:1], 0x38
	v_mov_b32_e32 v205, 0
	v_lshl_add_u64 v[146:147], s[6:7], 0, v[204:205]
	v_mov_b32_e32 v204, 0
	v_mov_b32_e32 v213, 0
	v_mov_b32_e32 v214, 0
	s_and_saveexec_b64 s[6:7], vcc
	s_cbranch_execz .LBB1_6
	global_load_dwordx4 v[238:241], v[146:147], off offset:1152
.LBB1_6:
	s_or_b64 exec, exec, s[6:7]
	v_mov_b32_e32 v202, 0
	s_and_saveexec_b64 s[6:7], s[4:5]
	s_cbranch_execz .LBB1_8
	global_load_dwordx4 v[242:245], v[146:147], off offset:1168

.LBB1_12:
	s_or_b64 exec, exec, s[8:9]
	s_waitcnt vmcnt(11)
	ds_write_b128 v215, v[146:149]
	s_waitcnt vmcnt(10)
	ds_write_b128 v216, v[150:153]
	s_waitcnt vmcnt(9)
	ds_write_b128 v217, v[154:157]
	s_waitcnt vmcnt(8)
	ds_write_b128 v218, v[158:161]
	s_waitcnt vmcnt(7)
	ds_write_b128 v219, v[162:165]
	s_waitcnt vmcnt(6)
	ds_write_b128 v220, v[166:169]
	s_waitcnt vmcnt(5)
	ds_write_b128 v221, v[170:173]
	s_waitcnt vmcnt(4)
	ds_write_b128 v222, v[174:177]
	s_waitcnt vmcnt(3)
	ds_write_b128 v223, v[178:181]
	s_waitcnt vmcnt(2)
	ds_write_b128 v224, v[182:185]
	s_waitcnt vmcnt(1)
	ds_write_b128 v226, v[190:193]
	s_waitcnt vmcnt(0)
	ds_write_b128 v227, v[194:197]
	s_and_saveexec_b64 s[6:7], vcc
	ds_write_b128 v225, v[186:189]
	s_or_b64 exec, exec, s[6:7]
	s_and_saveexec_b64 s[6:7], s[4:5]
	ds_write_b128 v228, v[198:201]
	s_or_b64 exec, exec, s[6:7]
	v_cvt_f16_f32_e32 v210, v230
	v_cvt_f16_f32_e32 v211, v233
	v_cvt_pk_f16_f32 v212, v231, v232
	v_cvt_pk_f16_f32 v203, v234, v235
	v_cvt_pk_f16_f32 v1, v236, v237
	v_cvt_f16_f32_e32 v204, v238
	v_cvt_f16_f32_e32 v213, v241
	v_cvt_pk_f16_f32 v214, v239, v240
	v_cvt_pk_f16_f32 v205, v242, v243
	v_cvt_pk_f16_f32 v202, v244, v245
	s_load_dwordx2 s[8:9], s[0:1], 0x18
	s_load_dwordx4 s[4:7], s[0:1], 0x28
	s_ashr_i32 s0, s2, 1
	s_and_b32 s17, s0, -8
	s_movk_i32 s0, 0x280
	v_cmp_gt_u32_e32 vcc, s0, v0
	s_and_saveexec_b64 s[0:1], vcc
	s_cbranch_execz .LBB1_21
	s_add_u32 s2, s10, s3
	s_addc_u32 s3, s11, 0
	s_mov_b64 s[10:11], 0
	s_movk_i32 s18, 0xffb0
	s_movk_i32 s19, 0x4b
	s_movk_i32 s20, 0x12c
	s_mov_b32 s21, 0x5040100
	s_mov_b32 s22, 0x1c400
	s_movk_i32 s23, 0x7f
	v_mov_b32_e32 v147, v0
	s_branch .LBB1_19
